# v65 + in-proj tile order r0: gelu,gelu,rope-k,rope-k; r1: rope-q,rope-q,gelu-stat,gelu-stat (gelu-stat stays on the converting workgroups, one round later)
# baseline (speedup 1.0000x reference)
;     __device__ bool next(int i, Unit& u) const { if (!base.next(i >> 1, u)) return false; if (i & 1) { u.pm += MTOK / BM; u.pn += DM / BM; } return true; }
;   __device__ __forceinline__ bool next(int i,AttnUnit&u)const{ if(i>=2||vcu>=256)return false; const int s=vcu&3; u.bh=vcu>>2; u.qb=(i==0)?7-s:s; return true; }
;     __host__ __device__ bool next(int i, Unit& u) const {
;         const int L = i * G + c; if (L >= nwg) return false;
;         int wgid = L; { const int q = nwg / NXCD, r = nwg % NXCD, xcd = wgid % NXCD, off = wgid / NXCD; wgid = (xcd < r ? xcd * (q + 1) : r * (q + 1) + (xcd - r) * q) + off; }
;         const int nig = WGM * nN, gid = wgid / nig, fm = gid * WGM, gsz = (nM - fm) < WGM ? (nM - fm) : WGM;
;         u.pm = fm + ((wgid % nig) % gsz); u.pn = (wgid % nig) / gsz; u.half = 0; return true;
.LBB0_382:
	s_ashr_i32 s4, s21, 31
	s_lshr_b32 s4, s4, 29
	s_add_i32 s4, s21, s4
	s_ashr_i32 s5, s4, 3
	s_and_b32 s4, s4, -8
	s_sub_i32 s4, s21, s4
	s_cmp_lt_i32 s4, 0
	s_movk_i32 s6, 0x91
	s_cselect_b32 s6, s6, 0x90
	s_mul_i32 s4, s4, s6
	s_add_i32 s4, s4, s5
	s_mul_hi_i32 s5, s4, 0x38e38e39
	s_lshr_b32 s6, s5, 31
	s_ashr_i32 s5, s5, 5
	s_add_i32 s5, s5, s6
	s_lshl_b32 s6, s5, 3
	s_mulk_i32 s5, 0x90
	s_sub_i32 s4, s4, s5
	s_bfe_u32 s5, s4, 0x3001c
	s_add_i32 s5, s4, s5
	s_sext_i32_i16 s7, s5
	s_and_b32 s5, s5, 0xfff8
	s_sub_i32 s4, s4, s5
	s_sext_i32_i16 s4, s4
	s_add_i32 s18, s6, s4
	s_ashr_i32 s70, s7, 3
	s_mul_i32 s4, s70, 5
	s_cmp_lt_u32 s70, 12
	s_cbranch_scc0 .Lpn_hi0
	s_mov_b32 s6, 0x8a439820
	s_mov_b32 s7, 0x5a92818
	s_branch .Lpn_go0

;     __device__ bool next(int i, Unit& u) const { if (!base.next(i >> 1, u)) return false; if (i & 1) { u.pm += MTOK / BM; u.pn += DM / BM; } return true; }
;   __device__ __forceinline__ bool next(int i,AttnUnit&u)const{ if(i>=2||vcu>=256)return false; const int s=vcu&3; u.bh=vcu>>2; u.qb=(i==0)?7-s:s; return true; }
;     __host__ __device__ bool next(int i, Unit& u) const {
;         const int L = i * G + c; if (L >= nwg) return false;
;         int wgid = L; { const int q = nwg / NXCD, r = nwg % NXCD, xcd = wgid % NXCD, off = wgid / NXCD; wgid = (xcd < r ? xcd * (q + 1) : r * (q + 1) + (xcd - r) * q) + off; }
;         const int nig = WGM * nN, gid = wgid / nig, fm = gid * WGM, gsz = (nM - fm) < WGM ? (nM - fm) : WGM;
;         u.pm = fm + ((wgid % nig) % gsz); u.pn = (wgid % nig) / gsz; u.half = 0; return true;
; template <class Epi, class Sched, bool ALIGN_EPI = false, bool SP2 = false>
; __device__ __forceinline__ void gemm_phase(PG8_LAS unsigned char* lds, const Gemm g, const Sched& S, const Epi& E) {
;     ...
;         const bool has_next = S.next(ui + 1, nxt);
;         const char* nA = has_next ? (const char*)g.A + (size_t)nxt.pm * tstep + (nxt.half == 2 ? hstep : (size_t)0) : cA; const char* nB = has_next ? (const char*)g.Bt + (size_t)nxt.pn * tstep : cB;
.LBB0_392:
	s_add_i32 s72, s72, 1
	s_mul_i32 s10, s72, s33
	s_add_i32 s10, s10, s21
	s_cmpk_lt_i32 s10, 0x480
	s_cselect_b64 s[64:65], -1, 0
	s_cmpk_gt_i32 s10, 0x47f
	s_cbranch_scc1 .LBB0_394
	s_ashr_i32 s11, s10, 31
	s_lshr_b32 s11, s11, 29
	s_add_i32 s11, s10, s11
	s_ashr_i32 s12, s11, 3
	s_and_b32 s11, s11, -8
	s_sub_i32 s10, s10, s11
	s_cmp_lt_i32 s10, 0
	s_movk_i32 s11, 0x91
	s_cselect_b32 s11, s11, 0x90
	s_mul_i32 s10, s10, s11
	s_add_i32 s10, s10, s12
	s_mul_hi_i32 s11, s10, 0x38e38e39
	s_lshr_b32 s12, s11, 31
	s_ashr_i32 s11, s11, 5
	s_add_i32 s11, s11, s12
	s_lshl_b32 s12, s11, 3
	s_mulk_i32 s11, 0x90
	s_sub_i32 s10, s10, s11
	s_bfe_u32 s11, s10, 0x3001c
	s_add_i32 s11, s10, s11
	s_sext_i32_i16 s13, s11
	s_and_b32 s11, s11, 0xfff8
	s_sub_i32 s10, s10, s11
	s_sext_i32_i16 s10, s10
	s_add_i32 s60, s12, s10
	s_ashr_i32 s62, s13, 3
	s_mul_i32 s10, s62, 5
	s_cmp_lt_u32 s62, 12
	s_cbranch_scc0 .Lpn_hi1
	s_mov_b32 s12, 0x8a439820
	s_mov_b32 s13, 0x5a92818
	s_branch .Lpn_go1
